# combine_norm and final moe_combine: norm gain vectors loaded once per phase into spare VGPRs (removes per-row load+wait chains that also forced the next rows prefetch to drain)
# speedup vs baseline: 1.0432x; 1.0019x over previous
.LBB0_513:
	s_and_b64 vcc, exec, s[26:27]
	s_cbranch_vccz .LBB0_524
	s_cmp_gt_i32 s91, 0
	s_mov_b64 s[26:27], -1
	s_cbranch_scc0 .LBB0_625
	s_cmp_gt_i32 s91, 1
	s_cbranch_scc0 .LBB0_526
	s_lshl_b32 s4, s72, 3
	v_readlane_b32 s14, v254, 32
	s_add_i32 s40, s4, s14
	s_cmpk_gt_i32 s40, 0x3fff
	v_readlane_b32 s15, v254, 33
	s_cbranch_scc1 .LBB0_525
	s_load_dwordx2 s[26:27], s[0:1], 0x98
	s_waitcnt vmcnt(0)
	v_ashrrev_i32_e32 v2, 3, v194
	v_ashrrev_i32_e32 v3, 31, v2
	v_lshlrev_b64 v[2:3], 2, v[2:3]
	s_mov_b64 s[16:17], 0x1800000
	s_waitcnt lgkmcnt(0)
	v_lshl_add_u64 v[4:5], s[26:27], 0, v[2:3]
	v_lshl_add_u64 v[50:51], v[4:5], 0, s[16:17]
	v_lshlrev_b32_e32 v4, 3, v194
	v_ashrrev_i32_e32 v5, 31, v4
	s_load_dwordx2 s[14:15], s[0:1], 0x40
	s_waitcnt vmcnt(14)
	v_lshlrev_b64 v[6:7], 1, v[4:5]
	s_add_u32 s36, s26, 0x23000000
	v_lshl_add_u64 v[8:9], s[26:27], 0, v[6:7]
	s_mov_b64 s[16:17], 0x20000000
	s_addc_u32 s37, s27, 0
	v_lshl_add_u64 v[52:53], v[8:9], 0, s[16:17]
	s_lshl_b32 s16, s82, 10
	s_ashr_i32 s17, s16, 31
	s_lshl_b64 s[16:17], s[16:17], 2
	s_waitcnt lgkmcnt(0)
	s_add_u32 s14, s14, s16
	s_addc_u32 s15, s15, s17
	s_add_i32 s5, s40, s88
	s_min_i32 s16, s5, 0x3fff
	s_ashr_i32 s17, s16, 31
	s_waitcnt vmcnt(13)
	v_lshlrev_b32_e32 v10, 2, v194
	s_lshl_b64 s[30:31], s[16:17], 10
	v_ashrrev_i32_e32 v11, 31, v10
	s_add_u32 s38, s36, s30
	s_addc_u32 s39, s37, s31
	v_lshlrev_b64 v[10:11], 1, v[10:11]
	s_ashr_i32 s41, s40, 31
	v_lshl_add_u64 v[12:13], s[38:39], 0, v[10:11]
	s_lshl_b64 s[38:39], s[40:41], 10
	s_add_u32 s42, s36, s38
	s_waitcnt vmcnt(10)
	v_lshl_add_u64 v[24:25], v[52:53], 0, s[30:31]
	s_brev_b32 s5, 64
	s_addc_u32 s43, s37, s39
	v_add_co_u32_e32 v18, vcc, s5, v24
	s_lshl_b64 s[16:17], s[16:17], 5
	s_nop 0
	v_addc_co_u32_e32 v19, vcc, 0, v25, vcc
	s_waitcnt vmcnt(8)
	v_lshl_add_u64 v[30:31], v[50:51], 0, s[16:17]
	s_mov_b32 s6, 0x100000
	v_add_co_u32_e32 v32, vcc, s6, v30
	s_mov_b32 s30, 0x1000000
	s_nop 0
	v_addc_co_u32_e32 v33, vcc, 0, v31, vcc
	v_add_co_u32_e32 v14, vcc, s30, v24
	s_mov_b32 s31, 0x80000
	s_nop 0
	v_addc_co_u32_e32 v15, vcc, 0, v25, vcc
	s_waitcnt vmcnt(7)
	v_add_co_u32_e32 v34, vcc, s31, v30
	global_load_dwordx4 v[14:17], v[14:15], off nt
	s_nop 0
	v_addc_co_u32_e32 v35, vcc, 0, v31, vcc
	global_load_dwordx4 v[18:21], v[18:19], off nt
	s_nop 0
	global_load_dwordx4 v[26:29], v[24:25], off nt
	v_lshl_add_u64 v[24:25], v[52:53], 0, s[38:39]
	v_add_co_u32_e32 v36, vcc, s5, v24
	s_lshl_b64 s[16:17], s[40:41], 5
	s_nop 0
	v_addc_co_u32_e32 v37, vcc, 0, v25, vcc
	v_lshl_add_u64 v[54:55], v[50:51], 0, s[16:17]
	v_add_co_u32_e32 v56, vcc, s6, v54
	v_lshl_add_u64 v[22:23], s[42:43], 0, v[10:11]
	s_nop 0
	v_addc_co_u32_e32 v57, vcc, 0, v55, vcc
	s_waitcnt vmcnt(9)
	v_add_co_u32_e32 v38, vcc, s30, v24
	v_ashrrev_i32_e32 v195, 31, v194
	s_nop 0
	v_addc_co_u32_e32 v39, vcc, 0, v25, vcc
	global_load_dwordx4 v[42:45], v[38:39], off nt
	s_nop 0
	global_load_dwordx4 v[38:41], v[36:37], off nt
	global_load_dwordx4 v[46:49], v[24:25], off nt
	v_add_co_u32_e32 v24, vcc, s31, v54
	v_readlane_b32 s5, v254, 28
	s_nop 0
	v_addc_co_u32_e32 v25, vcc, 0, v55, vcc
	global_load_dword v98, v[24:25], off
	global_load_dword v99, v[56:57], off
	global_load_dword v100, v[54:55], off
	global_load_dword v95, v[34:35], off
	global_load_dword v96, v[32:33], off
	global_load_dword v97, v[30:31], off
	global_load_dwordx2 v[74:75], v[12:13], off offset:512
	global_load_dwordx2 v[86:87], v[22:23], off offset:512
	global_load_dwordx2 v[88:89], v[22:23], off
	global_load_dwordx2 v[84:85], v[12:13], off
	v_lshl_add_u64 v[54:55], v[4:5], 2, s[14:15]
	v_lshlrev_b64 v[4:5], 4, v[194:195]
	v_sub_co_u32_e32 v4, vcc, 0, v4
	s_mov_b64 s[14:15], 0x24000000
	s_nop 0
	v_subb_co_u32_e32 v5, vcc, 0, v5, vcc
	v_lshl_add_u64 v[62:63], v[8:9], 0, s[14:15]
	s_lshl_b64 s[14:15], s[40:41], 11
	v_lshl_add_u64 v[56:57], v[54:55], 0, v[4:5]
	v_lshlrev_b64 v[4:5], 3, v[194:195]
	s_add_u32 s16, s14, 0x24000000
	v_sub_co_u32_e32 v60, vcc, 0, v4
	s_addc_u32 s17, s15, 0
	s_add_i32 s4, s5, s4
	v_subb_co_u32_e32 v61, vcc, 0, v5, vcc
	v_lshl_add_u64 v[8:9], s[14:15], 0, v[6:7]
	s_ashr_i32 s5, s4, 31
	s_waitcnt vmcnt(19)
	v_sub_co_u32_e32 v66, vcc, v8, v4
	s_lshl_b64 s[14:15], s[4:5], 10
	s_lshl_b64 s[4:5], s[4:5], 5
	v_lshl_add_u64 v[58:59], s[36:37], 0, v[10:11]
	v_lshl_add_u64 v[64:65], s[16:17], 0, v[6:7]
	v_subb_co_u32_e32 v67, vcc, v9, v5, vcc
	v_lshl_add_u64 v[68:69], s[14:15], 0, v[10:11]
	s_waitcnt vmcnt(18)
	v_lshl_add_u64 v[70:71], s[14:15], 0, v[6:7]
	v_lshl_add_u64 v[72:73], s[4:5], 0, v[2:3]
	s_waitcnt vmcnt(15)
	v_mov_b64_e32 v[32:33], v[16:17]
	v_mov_b64_e32 v[30:31], v[14:15]
	s_waitcnt vmcnt(14)
	v_mov_b64_e32 v[36:37], v[20:21]
	s_waitcnt vmcnt(13)
	v_mov_b64_e32 v[22:23], v[26:27]
	v_mov_b64_e32 v[24:25], v[28:29]
	v_mov_b64_e32 v[34:35], v[18:19]
	s_waitcnt vmcnt(9)
	v_mov_b32_e32 v90, v98
	v_mov_b64_e32 v[6:7], v[42:43]
	v_mov_b64_e32 v[10:11], v[38:39]
	v_mov_b64_e32 v[2:3], v[46:47]
	v_mov_b64_e32 v[4:5], v[48:49]
	v_mov_b64_e32 v[8:9], v[44:45]
	v_mov_b64_e32 v[12:13], v[40:41]
	s_waitcnt vmcnt(7)
	v_mov_b32_e32 v0, v100
	v_mov_b32_e32 v91, v99
	s_waitcnt vmcnt(4)
	v_mov_b32_e32 v92, v97
	v_mov_b32_e32 v93, v95
	v_mov_b32_e32 v94, v96
	global_load_dwordx4 v[130:133], v[54:55], off offset:16
	global_load_dwordx4 v[134:137], v[54:55], off
	global_load_dwordx4 v[138:141], v[56:57], off offset:2048
	global_load_dwordx4 v[142:145], v[56:57], off offset:3072
	s_waitcnt vmcnt(0)
	s_branch .LBB0_519
.LBB0_518:
	s_waitcnt vmcnt(3)
	v_readlane_b32 s14, v255, 1
	v_readlane_b32 s15, v255, 2
	v_mov_b64_e32 v[48:49], v[4:5]
	v_mov_b64_e32 v[44:45], v[8:9]
	v_lshl_add_u64 v[64:65], v[64:65], 0, s[14:15]
	v_lshl_add_u64 v[66:67], v[66:67], 0, s[14:15]
	v_readlane_b32 s14, v255, 3
	v_readlane_b32 s15, v255, 4
	v_mov_b64_e32 v[40:41], v[12:13]
	v_mov_b64_e32 v[28:29], v[24:25]
	v_lshl_add_u64 v[68:69], v[68:69], 0, s[14:15]
	v_lshl_add_u64 v[70:71], v[70:71], 0, s[14:15]
	v_readlane_b32 s14, v255, 5
	v_readlane_b32 s15, v255, 6
	v_mov_b64_e32 v[14:15], v[30:31]
	v_mov_b64_e32 v[18:19], v[34:35]
	v_lshl_add_u64 v[72:73], v[72:73], 0, s[14:15]
	s_and_b64 vcc, exec, s[36:37]
	v_mov_b64_e32 v[46:47], v[2:3]
	v_mov_b64_e32 v[42:43], v[6:7]
	v_mov_b64_e32 v[38:39], v[10:11]
	v_mov_b64_e32 v[26:27], v[22:23]
	v_mov_b64_e32 v[16:17], v[32:33]
	v_mov_b64_e32 v[20:21], v[36:37]
	v_mov_b32_e32 v100, v0
	v_mov_b32_e32 v98, v90
	v_mov_b32_e32 v99, v91
	v_mov_b32_e32 v97, v92
	v_mov_b32_e32 v95, v93
	v_mov_b32_e32 v96, v94
	s_mov_b32 s40, s4
	v_mov_b32_e32 v88, v76
	v_mov_b32_e32 v89, v77
	v_mov_b32_e32 v84, v82
	v_mov_b32_e32 v85, v83
	v_mov_b32_e32 v86, v78
	v_mov_b32_e32 v87, v79
	v_mov_b32_e32 v74, v80
	v_mov_b32_e32 v75, v81
	s_cbranch_vccnz .LBB0_525
.LBB0_519:
	s_add_i32 s4, s40, s90
	s_cmpk_gt_i32 s4, 0x3fff
	s_cselect_b64 s[36:37], -1, 0
	s_and_b64 vcc, exec, s[36:37]
	s_waitcnt vmcnt(3)
	v_mov_b32_e32 v78, v86
	v_mov_b32_e32 v79, v87
	v_mov_b32_e32 v80, v74
	v_mov_b32_e32 v81, v75
	v_mov_b32_e32 v76, v88
	v_mov_b32_e32 v77, v89
	v_mov_b32_e32 v82, v84
	v_mov_b32_e32 v83, v85
	s_cbranch_vccnz .LBB0_521
	v_lshl_add_u64 v[6:7], s[26:27], 0, v[72:73]
	v_add_co_u32_e32 v2, vcc, 0x1800000, v6
	v_lshl_add_u64 v[10:11], s[26:27], 0, v[70:71]
	s_nop 0
	v_addc_co_u32_e32 v3, vcc, 0, v7, vcc
	v_add_co_u32_e32 v4, vcc, 0x20000000, v10
	s_mul_i32 s5, s76, 24
	s_nop 0
	v_addc_co_u32_e32 v5, vcc, 0, v11, vcc
	v_add_co_u32_e32 v8, vcc, 0x1880000, v6
	s_add_i32 s5, s5, s40
	s_nop 0
	v_addc_co_u32_e32 v9, vcc, 0, v7, vcc
	global_load_dword v0, v[2:3], off
	s_nop 0
	global_load_dwordx4 v[2:5], v[4:5], off nt
	s_nop 0
	global_load_dword v90, v[8:9], off
	v_add_co_u32_e32 v8, vcc, 0x21000000, v10
	s_min_i32 s14, s5, 0x3fff
	s_nop 0
	v_addc_co_u32_e32 v9, vcc, 0, v11, vcc
	v_add_co_u32_e32 v12, vcc, 0x1900000, v6
	s_ashr_i32 s15, s14, 31
	s_nop 0
	v_addc_co_u32_e32 v13, vcc, 0, v7, vcc
	v_add_co_u32_e32 v10, vcc, 0x22000000, v10
	global_load_dwordx4 v[6:9], v[8:9], off nt
	s_nop 0
	global_load_dword v91, v[12:13], off
	v_addc_co_u32_e32 v11, vcc, 0, v11, vcc
	v_lshl_add_u64 v[12:13], s[26:27], 0, v[68:69]
	v_add_co_u32_e32 v22, vcc, 0x23000000, v12
	s_lshl_b64 s[16:17], s[14:15], 5
	s_nop 0
	v_addc_co_u32_e32 v23, vcc, 0, v13, vcc
	v_lshl_add_u64 v[30:31], v[50:51], 0, s[16:17]
	s_lshl_b64 s[14:15], s[14:15], 10
	v_add_co_u32_e32 v32, vcc, 0x80000, v30
	v_lshl_add_u64 v[34:35], v[52:53], 0, s[14:15]
	s_nop 0
	v_addc_co_u32_e32 v33, vcc, 0, v31, vcc
	global_load_dwordx4 v[10:13], v[10:11], off nt
	s_nop 0
	global_load_dwordx2 v[76:77], v[22:23], off
	global_load_dwordx2 v[78:79], v[22:23], off offset:512
	global_load_dword v92, v[30:31], off
	s_nop 0
	global_load_dwordx4 v[22:25], v[34:35], off nt
	global_load_dword v93, v[32:33], off
	v_add_co_u32_e32 v32, vcc, 0x1000000, v34
	v_lshl_add_u64 v[80:81], v[58:59], 0, s[14:15]
	s_nop 0
	v_addc_co_u32_e32 v33, vcc, 0, v35, vcc
	v_add_co_u32_e32 v36, vcc, 0x100000, v30
	s_nop 1
	v_addc_co_u32_e32 v37, vcc, 0, v31, vcc
	v_add_co_u32_e32 v34, vcc, 0x2000000, v34
	global_load_dwordx4 v[30:33], v[32:33], off nt
	s_nop 0
	global_load_dword v94, v[36:37], off
	v_addc_co_u32_e32 v35, vcc, 0, v35, vcc
	global_load_dwordx4 v[34:37], v[34:35], off nt
	s_nop 0
	global_load_dwordx2 v[82:83], v[80:81], off
	s_nop 0
	global_load_dwordx2 v[80:81], v[80:81], off offset:512
.LBB0_521:
	v_max3_f32 v101, v100, v98, v99
	v_sub_f32_e32 v100, v100, v101
	v_sub_f32_e32 v98, v98, v101
	v_exp_f32_e32 v115, v100
	v_exp_f32_e32 v114, v98
	v_sub_f32_e32 v98, v99, v101
	v_exp_f32_e32 v106, v98
	v_lshlrev_b32_e32 v124, 16, v49
	v_add_f32_e32 v98, v115, v114
	v_and_b32_e32 v125, 0xffff0000, v45
	v_add_f32_e32 v98, v106, v98
	v_div_scale_f32 v99, s[14:15], v98, v98, 1.0
	v_rcp_f32_e32 v100, v99
	v_and_b32_e32 v127, 0xffff0000, v48
	v_lshlrev_b32_e32 v48, 16, v48
	v_lshlrev_b32_e32 v126, 16, v44
	v_fma_f32 v101, -v99, v100, 1.0
	v_fmac_f32_e32 v100, v101, v100
	v_div_scale_f32 v101, vcc, 1.0, v98, 1.0
	v_mul_f32_e32 v102, v101, v100
	v_fma_f32 v103, -v99, v102, v101
	v_fmac_f32_e32 v102, v103, v100
	v_fma_f32 v99, -v99, v102, v101
	v_div_fmas_f32 v99, v99, v100, v102
	v_div_fixup_f32 v116, v99, v98, 1.0
	v_mul_f32_e32 v118, v106, v116
	v_pk_mul_f32 v[114:115], v[114:115], v[116:117] op_sel_hi:[1,0]
	v_lshlrev_b32_e32 v116, 16, v45
	v_and_b32_e32 v117, 0xffff0000, v49
	v_pk_mul_f32 v[124:125], v[114:115], v[124:125] op_sel:[1,0] op_sel_hi:[0,1]
	v_and_b32_e32 v49, 0xffff0000, v44
	v_pk_fma_f32 v[116:117], v[114:115], v[116:117], v[124:125]
	v_lshlrev_b32_e32 v124, 16, v41
	v_and_b32_e32 v125, 0xffff0000, v41
	v_lshlrev_b32_e32 v44, 16, v40
	v_and_b32_e32 v45, 0xffff0000, v40
	v_pk_mul_f32 v[40:41], v[114:115], v[48:49] op_sel:[1,0] op_sel_hi:[0,1]
	v_pk_fma_f32 v[40:41], v[114:115], v[126:127], v[40:41]
	v_lshlrev_b32_e32 v126, 16, v47
	v_and_b32_e32 v127, 0xffff0000, v43
	v_lshlrev_b32_e32 v48, 16, v43
	v_and_b32_e32 v49, 0xffff0000, v47
	v_pk_mul_f32 v[126:127], v[114:115], v[126:127] op_sel:[1,0] op_sel_hi:[0,1]
	v_lshlrev_b32_e32 v128, 16, v39
	v_and_b32_e32 v129, 0xffff0000, v39
	v_pk_fma_f32 v[48:49], v[114:115], v[48:49], v[126:127]
	v_and_b32_e32 v47, 0xffff0000, v42
	v_pk_fma_f32 v[48:49], v[118:119], v[128:129], v[48:49] op_sel_hi:[0,1,1]
	v_and_b32_e32 v129, 0xffff0000, v46
	v_lshlrev_b32_e32 v46, 16, v46
	v_lshlrev_b32_e32 v128, 16, v42
	v_lshlrev_b32_e32 v42, 16, v38
	v_and_b32_e32 v43, 0xffff0000, v38
	v_pk_mul_f32 v[38:39], v[114:115], v[46:47] op_sel:[1,0] op_sel_hi:[0,1]
	v_pk_fma_f32 v[38:39], v[114:115], v[128:129], v[38:39]
	v_pk_fma_f32 v[40:41], v[118:119], v[44:45], v[40:41] op_sel_hi:[0,1,1]
	v_pk_fma_f32 v[38:39], v[118:119], v[42:43], v[38:39] op_sel_hi:[0,1,1]
	v_pk_mul_f32 v[126:127], v[48:49], v[48:49]
	v_pk_mul_f32 v[42:43], v[38:39], v[38:39]
	v_pk_fma_f32 v[116:117], v[118:119], v[124:125], v[116:117] op_sel_hi:[0,1,1]
	v_pk_mul_f32 v[44:45], v[40:41], v[40:41]
	v_add_f32_e32 v46, v127, v126
	v_add_f32_e32 v42, v43, v42
	v_pk_mul_f32 v[124:125], v[116:117], v[116:117]
	v_add_f32_e32 v42, v42, v46
	v_add_f32_e32 v43, v45, v44
	v_add_f32_e32 v42, v43, v42
	v_add_f32_e32 v43, v125, v124
	v_add_f32_e32 v42, v43, v42
	v_lshlrev_b32_e32 v120, 16, v88
	v_and_b32_e32 v121, 0xffff0000, v88
	v_add_f32_dpp v42, v42, v42 quad_perm:[1,0,3,2] row_mask:0xf bank_mask:0xf bound_ctrl:1
	v_lshlrev_b32_e32 v88, 16, v89
	v_and_b32_e32 v89, 0xffff0000, v89
	v_add_f32_dpp v42, v42, v42 quad_perm:[2,3,0,1] row_mask:0xf bank_mask:0xf bound_ctrl:1
	v_lshlrev_b32_e32 v122, 16, v86
	v_and_b32_e32 v123, 0xffff0000, v86
	v_add_f32_dpp v42, v42, v42 row_half_mirror row_mask:0xf bank_mask:0xf bound_ctrl:1
	s_mov_b32 s6, 0x3b800000
	s_brev_b32 s5, 36
	v_add_f32_dpp v42, v42, v42 row_mirror row_mask:0xf bank_mask:0xf bound_ctrl:1
	v_mov_b32_e32 v43, v42
	s_nop 1
	v_permlane16_swap_b32_e32 v42, v43
	v_add_f32_e32 v42, v42, v43
	v_mov_b32_e32 v43, v42
	s_nop 1
	v_permlane32_swap_b32_e32 v42, v43
	v_add_f32_e32 v42, v42, v43
	v_fmamk_f32 v42, v42, 0x3b000000, v190
	v_mul_f32_e32 v43, 0x4b800000, v42
	v_cmp_gt_f32_e32 vcc, s96, v42
	s_nop 1
	v_cndmask_b32_e32 v42, v42, v43, vcc
	v_rsq_f32_e32 v44, v42
	v_lshlrev_b32_e32 v42, 16, v87
	v_and_b32_e32 v43, 0xffff0000, v87
	v_pk_mul_f32 v[86:87], v[122:123], v[122:123]
	v_mul_f32_e32 v45, 0x45800000, v44
	v_cndmask_b32_e32 v44, v44, v45, vcc
	v_pk_mul_f32 v[38:39], v[38:39], v[44:45] op_sel_hi:[1,0]
	v_pk_mul_f32 v[46:47], v[48:49], v[44:45] op_sel_hi:[1,0]
	v_pk_mul_f32 v[38:39], v[38:39], v[134:135]
	v_pk_mul_f32 v[46:47], v[46:47], v[136:137]
	v_pk_mul_f32 v[40:41], v[40:41], v[44:45] op_sel_hi:[1,0]
	v_pk_mul_f32 v[44:45], v[116:117], v[44:45] op_sel_hi:[1,0]
	v_cvt_pk_bf16_f32 v38, v38, v39
	v_cvt_pk_bf16_f32 v39, v46, v47
	v_pk_mul_f32 v[40:41], v[40:41], v[130:131]
	v_pk_mul_f32 v[44:45], v[44:45], v[132:133]
	v_pk_mul_f32 v[46:47], v[120:121], v[120:121]
	v_cvt_pk_bf16_f32 v40, v40, v41
	v_cvt_pk_bf16_f32 v41, v44, v45
	v_pk_mul_f32 v[44:45], v[88:89], v[88:89]
	v_add_f32_e32 v46, v46, v47
	v_add_f32_e32 v44, v44, v46
	v_add_f32_e32 v44, v45, v44
	v_pk_mul_f32 v[48:49], v[42:43], v[42:43]
	s_nop 0
	v_add_f32_dpp v44, v44, v44 quad_perm:[1,0,3,2] row_mask:0xf bank_mask:0xf bound_ctrl:1
	s_nop 1
	v_add_f32_dpp v44, v44, v44 quad_perm:[2,3,0,1] row_mask:0xf bank_mask:0xf bound_ctrl:1
	s_nop 1
	v_add_f32_dpp v44, v44, v44 row_half_mirror row_mask:0xf bank_mask:0xf bound_ctrl:1
	s_nop 1
	v_add_f32_dpp v44, v44, v44 row_mirror row_mask:0xf bank_mask:0xf bound_ctrl:1
	v_mov_b32_e32 v45, v44
	s_nop 1
	v_permlane16_swap_b32_e32 v44, v45
	v_add_f32_e32 v45, v44, v45
	v_add_f32_e32 v44, v86, v87
	v_add_f32_e32 v44, v48, v44
	v_add_f32_e32 v44, v49, v44
	v_mov_b32_e32 v47, v45
	s_nop 1
	v_permlane32_swap_b32_e32 v45, v47
	v_add_f32_dpp v44, v44, v44 quad_perm:[1,0,3,2] row_mask:0xf bank_mask:0xf bound_ctrl:1
	s_nop 1
	v_add_f32_dpp v44, v44, v44 quad_perm:[2,3,0,1] row_mask:0xf bank_mask:0xf bound_ctrl:1
	s_nop 1
	v_add_f32_dpp v44, v44, v44 row_half_mirror row_mask:0xf bank_mask:0xf bound_ctrl:1
	s_nop 1
	v_add_f32_dpp v44, v44, v44 row_mirror row_mask:0xf bank_mask:0xf bound_ctrl:1
	v_mov_b32_e32 v46, v44
	s_nop 1
	v_permlane16_swap_b32_e32 v44, v46
	v_add_f32_e32 v44, v44, v46
	v_mov_b32_e32 v46, v44
	s_nop 1
	v_permlane32_swap_b32_e32 v44, v46
	v_pk_add_f32 v[44:45], v[44:45], v[46:47]
	s_nop 0
	v_pk_fma_f32 v[44:45], v[44:45], s[6:7], v[190:191] op_sel_hi:[1,0,0]
	s_nop 0
	v_mul_f32_e32 v46, 0x4b800000, v45
	v_cmp_gt_f32_e32 vcc, s96, v45
	s_nop 1
	v_cndmask_b32_e32 v45, v45, v46, vcc
	v_rsq_f32_e32 v45, v45
	v_lshl_add_u64 v[46:47], s[26:27], 0, v[64:65]
	global_store_dwordx4 v[46:47], v[38:41], off
	s_nop 1
	v_mul_f32_e32 v40, 0x45800000, v45
	v_cndmask_b32_e32 v40, v45, v40, vcc
	v_pk_mul_f32 v[46:47], v[40:41], v[120:121] op_sel_hi:[0,1]
	v_pk_mul_f32 v[40:41], v[40:41], v[88:89] op_sel_hi:[0,1]
	v_pk_mul_f32 v[46:47], v[138:139], v[46:47]
	v_pk_mul_f32 v[40:41], v[140:141], v[40:41]
	v_cvt_pk_bf16_f32 v46, v46, v47
	v_cvt_pk_bf16_f32 v47, v40, v41
	v_mul_f32_e32 v40, 0x4b800000, v44
	v_cmp_gt_f32_e32 vcc, s96, v44
	v_lshl_add_u64 v[38:39], s[26:27], 0, v[66:67]
	v_add_co_u32_e64 v38, s[38:39], s5, v38
	v_cndmask_b32_e32 v40, v44, v40, vcc
	v_rsq_f32_e32 v40, v40
	v_addc_co_u32_e64 v39, s[38:39], 0, v39, s[38:39]
	s_add_i32 s38, s88, s40
	v_mul_f32_e32 v41, 0x45800000, v40
	v_cndmask_b32_e32 v40, v40, v41, vcc
	v_pk_mul_f32 v[44:45], v[40:41], v[122:123] op_sel_hi:[0,1]
	v_pk_mul_f32 v[40:41], v[40:41], v[42:43] op_sel_hi:[0,1]
	v_pk_mul_f32 v[44:45], v[142:143], v[44:45]
	v_pk_mul_f32 v[40:41], v[144:145], v[40:41]
	v_cvt_pk_bf16_f32 v44, v44, v45
	v_cvt_pk_bf16_f32 v45, v40, v41
	s_cmpk_gt_i32 s38, 0x3fff
	global_store_dwordx2 v[38:39], v[46:47], off offset:1024
	global_store_dwordx2 v[38:39], v[44:45], off offset:1536
	s_cbranch_scc1 .LBB0_518
	v_max3_f32 v38, v97, v95, v96
	v_sub_f32_e32 v39, v97, v38
	v_exp_f32_e32 v89, v39
	v_sub_f32_e32 v39, v95, v38
	v_exp_f32_e32 v88, v39
	v_sub_f32_e32 v38, v96, v38
	v_exp_f32_e32 v38, v38
	v_lshlrev_b32_e32 v100, 16, v84
	v_add_f32_e32 v39, v89, v88
	v_and_b32_e32 v101, 0xffff0000, v84
	v_add_f32_e32 v39, v38, v39
	v_div_scale_f32 v40, s[14:15], v39, v39, 1.0
	v_rcp_f32_e32 v41, v40
	v_lshlrev_b32_e32 v102, 16, v85
	v_and_b32_e32 v103, 0xffff0000, v85
	v_lshlrev_b32_e32 v106, 16, v29
	v_fma_f32 v42, -v40, v41, 1.0
	v_fmac_f32_e32 v41, v42, v41
	v_div_scale_f32 v42, vcc, 1.0, v39, 1.0
	v_mul_f32_e32 v43, v42, v41
	v_fma_f32 v44, -v40, v43, v42
	v_fmac_f32_e32 v43, v44, v41
	v_fma_f32 v40, -v40, v43, v42
	v_div_fmas_f32 v40, v40, v41, v43
	v_div_fixup_f32 v96, v40, v39, 1.0
	v_mul_f32_e32 v98, v38, v96
	v_pk_mul_f32 v[88:89], v[88:89], v[96:97] op_sel_hi:[1,0]
	v_and_b32_e32 v107, 0xffff0000, v17
	v_lshlrev_b32_e32 v96, 16, v17
	v_and_b32_e32 v97, 0xffff0000, v29
	v_pk_mul_f32 v[106:107], v[88:89], v[106:107] op_sel:[1,0] op_sel_hi:[0,1]
	v_and_b32_e32 v109, 0xffff0000, v28
	v_lshlrev_b32_e32 v28, 16, v28
	v_and_b32_e32 v29, 0xffff0000, v16
	v_pk_fma_f32 v[96:97], v[88:89], v[96:97], v[106:107]
	v_lshlrev_b32_e32 v106, 16, v21
	v_and_b32_e32 v107, 0xffff0000, v21
	v_lshlrev_b32_e32 v108, 16, v16
	v_lshlrev_b32_e32 v16, 16, v20
	v_and_b32_e32 v17, 0xffff0000, v20
	v_pk_mul_f32 v[20:21], v[88:89], v[28:29] op_sel:[1,0] op_sel_hi:[0,1]
	v_pk_fma_f32 v[20:21], v[88:89], v[108:109], v[20:21]
	v_lshlrev_b32_e32 v108, 16, v27
	v_and_b32_e32 v109, 0xffff0000, v15
	v_lshlrev_b32_e32 v28, 16, v15
	v_and_b32_e32 v29, 0xffff0000, v27
	v_pk_mul_f32 v[108:109], v[88:89], v[108:109] op_sel:[1,0] op_sel_hi:[0,1]
	v_lshlrev_b32_e32 v110, 16, v19
	v_and_b32_e32 v111, 0xffff0000, v19
	v_pk_fma_f32 v[28:29], v[88:89], v[28:29], v[108:109]
	v_and_b32_e32 v27, 0xffff0000, v14
	v_pk_fma_f32 v[28:29], v[98:99], v[110:111], v[28:29] op_sel_hi:[0,1,1]
	v_and_b32_e32 v111, 0xffff0000, v26
	v_lshlrev_b32_e32 v26, 16, v26
	v_lshlrev_b32_e32 v110, 16, v14
	v_lshlrev_b32_e32 v14, 16, v18
	v_and_b32_e32 v15, 0xffff0000, v18
	v_pk_mul_f32 v[18:19], v[88:89], v[26:27] op_sel:[1,0] op_sel_hi:[0,1]
	v_pk_fma_f32 v[18:19], v[88:89], v[110:111], v[18:19]
	v_pk_fma_f32 v[16:17], v[98:99], v[16:17], v[20:21] op_sel_hi:[0,1,1]
	v_pk_fma_f32 v[14:15], v[98:99], v[14:15], v[18:19] op_sel_hi:[0,1,1]
	v_pk_mul_f32 v[108:109], v[28:29], v[28:29]
	v_pk_mul_f32 v[18:19], v[14:15], v[14:15]
	v_pk_fma_f32 v[96:97], v[98:99], v[106:107], v[96:97] op_sel_hi:[0,1,1]
	v_pk_mul_f32 v[20:21], v[16:17], v[16:17]
	v_add_f32_e32 v26, v109, v108
	v_add_f32_e32 v18, v19, v18
	v_pk_mul_f32 v[106:107], v[96:97], v[96:97]
	v_add_f32_e32 v18, v18, v26
	v_add_f32_e32 v19, v21, v20
	v_add_f32_e32 v18, v19, v18
	v_add_f32_e32 v19, v107, v106
	v_add_f32_e32 v18, v19, v18
	v_lshlrev_b32_e32 v104, 16, v74
	v_and_b32_e32 v105, 0xffff0000, v74
	v_add_f32_dpp v18, v18, v18 quad_perm:[1,0,3,2] row_mask:0xf bank_mask:0xf bound_ctrl:1
	s_ashr_i32 s39, s38, 31
	s_lshl_b64 s[14:15], s[38:39], 11
	v_add_f32_dpp v18, v18, v18 quad_perm:[2,3,0,1] row_mask:0xf bank_mask:0xf bound_ctrl:1
	s_nop 1
	v_add_f32_dpp v18, v18, v18 row_half_mirror row_mask:0xf bank_mask:0xf bound_ctrl:1
	s_nop 1
	v_add_f32_dpp v18, v18, v18 row_mirror row_mask:0xf bank_mask:0xf bound_ctrl:1
	v_mov_b32_e32 v19, v18
	s_nop 1
	v_permlane16_swap_b32_e32 v18, v19
	v_add_f32_e32 v18, v18, v19
	v_mov_b32_e32 v19, v18
	s_nop 1
	v_permlane32_swap_b32_e32 v18, v19
	v_add_f32_e32 v18, v18, v19
	v_fmamk_f32 v18, v18, 0x3b000000, v190
	v_mul_f32_e32 v19, 0x4b800000, v18
	v_cmp_gt_f32_e32 vcc, s96, v18
	s_nop 1
	v_cndmask_b32_e32 v18, v18, v19, vcc
	v_rsq_f32_e32 v20, v18
	v_lshlrev_b32_e32 v18, 16, v75
	v_and_b32_e32 v19, 0xffff0000, v75
	v_mul_f32_e32 v21, 0x45800000, v20
	v_cndmask_b32_e32 v20, v20, v21, vcc
	v_pk_mul_f32 v[14:15], v[14:15], v[20:21] op_sel_hi:[1,0]
	v_pk_mul_f32 v[26:27], v[28:29], v[20:21] op_sel_hi:[1,0]
	v_pk_mul_f32 v[14:15], v[14:15], v[134:135]
	v_pk_mul_f32 v[26:27], v[26:27], v[136:137]
	v_pk_mul_f32 v[16:17], v[16:17], v[20:21] op_sel_hi:[1,0]
	v_pk_mul_f32 v[20:21], v[96:97], v[20:21] op_sel_hi:[1,0]
	v_cvt_pk_bf16_f32 v14, v14, v15
	v_cvt_pk_bf16_f32 v15, v26, v27
	v_pk_mul_f32 v[16:17], v[16:17], v[130:131]
	v_pk_mul_f32 v[20:21], v[20:21], v[132:133]
	v_pk_mul_f32 v[26:27], v[100:101], v[100:101]
	v_cvt_pk_bf16_f32 v16, v16, v17
	v_cvt_pk_bf16_f32 v17, v20, v21
	v_pk_mul_f32 v[20:21], v[102:103], v[102:103]
	v_add_f32_e32 v26, v26, v27
	v_add_f32_e32 v20, v20, v26
	v_add_f32_e32 v20, v21, v20
	v_pk_mul_f32 v[38:39], v[104:105], v[104:105]
	v_pk_mul_f32 v[28:29], v[18:19], v[18:19]
	v_add_f32_dpp v20, v20, v20 quad_perm:[1,0,3,2] row_mask:0xf bank_mask:0xf bound_ctrl:1
	s_nop 1
	v_add_f32_dpp v20, v20, v20 quad_perm:[2,3,0,1] row_mask:0xf bank_mask:0xf bound_ctrl:1
	s_nop 1
	v_add_f32_dpp v20, v20, v20 row_half_mirror row_mask:0xf bank_mask:0xf bound_ctrl:1
	s_nop 1
	v_add_f32_dpp v20, v20, v20 row_mirror row_mask:0xf bank_mask:0xf bound_ctrl:1
	v_mov_b32_e32 v21, v20
	s_nop 1
	v_permlane16_swap_b32_e32 v20, v21
	v_add_f32_e32 v21, v20, v21
	v_add_f32_e32 v20, v38, v39
	v_add_f32_e32 v20, v28, v20
	v_add_f32_e32 v20, v29, v20
	v_mov_b32_e32 v27, v21
	s_nop 1
	v_permlane32_swap_b32_e32 v21, v27
	v_add_f32_dpp v20, v20, v20 quad_perm:[1,0,3,2] row_mask:0xf bank_mask:0xf bound_ctrl:1
	s_nop 1
	v_add_f32_dpp v20, v20, v20 quad_perm:[2,3,0,1] row_mask:0xf bank_mask:0xf bound_ctrl:1
	s_nop 1
	v_add_f32_dpp v20, v20, v20 row_half_mirror row_mask:0xf bank_mask:0xf bound_ctrl:1
	s_nop 1
	v_add_f32_dpp v20, v20, v20 row_mirror row_mask:0xf bank_mask:0xf bound_ctrl:1
	v_mov_b32_e32 v26, v20
	s_nop 1
	v_permlane16_swap_b32_e32 v20, v26
	v_add_f32_e32 v20, v20, v26
	v_mov_b32_e32 v26, v20
	s_nop 1
	v_permlane32_swap_b32_e32 v20, v26
	v_pk_add_f32 v[20:21], v[20:21], v[26:27]
	s_nop 0
	v_pk_fma_f32 v[20:21], v[20:21], s[6:7], v[190:191] op_sel_hi:[1,0,0]
	s_nop 0
	v_mul_f32_e32 v26, 0x4b800000, v21
	v_cmp_gt_f32_e32 vcc, s96, v21
	s_nop 1
	v_cndmask_b32_e32 v21, v21, v26, vcc
	v_rsq_f32_e32 v21, v21
	v_lshl_add_u64 v[26:27], v[62:63], 0, s[14:15]
	global_store_dwordx4 v[26:27], v[14:17], off
	s_nop 1
	v_mul_f32_e32 v16, 0x45800000, v21
	v_cndmask_b32_e32 v16, v21, v16, vcc
	v_mul_f32_e32 v21, 0x4b800000, v20
	v_cmp_gt_f32_e32 vcc, s96, v20
	v_lshl_add_u64 v[14:15], v[26:27], 0, v[60:61]
	v_pk_mul_f32 v[26:27], v[16:17], v[100:101] op_sel_hi:[0,1]
	v_cndmask_b32_e32 v20, v20, v21, vcc
	v_rsq_f32_e32 v20, v20
	v_pk_mul_f32 v[16:17], v[16:17], v[102:103] op_sel_hi:[0,1]
	v_pk_mul_f32 v[26:27], v[138:139], v[26:27]
	v_pk_mul_f32 v[16:17], v[140:141], v[16:17]
	v_cvt_pk_bf16_f32 v26, v26, v27
	v_cvt_pk_bf16_f32 v27, v16, v17
	v_mul_f32_e32 v16, 0x45800000, v20
	v_cndmask_b32_e32 v16, v20, v16, vcc
	v_pk_mul_f32 v[20:21], v[16:17], v[104:105] op_sel_hi:[0,1]
	v_pk_mul_f32 v[16:17], v[16:17], v[18:19] op_sel_hi:[0,1]
	v_pk_mul_f32 v[20:21], v[142:143], v[20:21]
	v_pk_mul_f32 v[16:17], v[144:145], v[16:17]
	v_cvt_pk_bf16_f32 v20, v20, v21
	v_cvt_pk_bf16_f32 v21, v16, v17
	global_store_dwordx2 v[14:15], v[26:27], off offset:1024
	global_store_dwordx2 v[14:15], v[20:21], off offset:1536
	s_branch .LBB0_518

.LBB0_638:
	s_lshl_b32 s4, s72, 3
	v_readlane_b32 s14, v254, 32
	s_add_i32 s40, s4, s14
	s_cmpk_gt_i32 s40, 0x3fff
	v_readlane_b32 s15, v254, 33
	s_cbranch_scc1 .LBB0_654
	s_waitcnt lgkmcnt(0)
	s_add_u32 s5, s26, 0x1600000
	s_addc_u32 s6, s27, 0
	s_add_u32 s14, s26, 0x1640000
	s_addc_u32 s15, s27, 0
	s_add_u32 s16, s26, 0x1680000
	s_addc_u32 s17, s27, 0
	s_add_i32 s4, s40, s88
	s_min_i32 s38, s4, 0x3fff
	s_ashr_i32 s39, s38, 31
	s_lshl_b64 s[38:39], s[38:39], 4
	s_add_u32 s42, s16, s38
	s_addc_u32 s43, s17, s39
	global_load_dwordx4 v[22:25], v1, s[42:43]
	s_add_u32 s42, s14, s38
	s_addc_u32 s43, s15, s39
	s_add_u32 s38, s5, s38
	s_addc_u32 s39, s6, s39
	s_ashr_i32 s41, s40, 31
	global_load_dwordx4 v[2:5], v1, s[42:43]
	global_load_dwordx4 v[6:9], v1, s[38:39]
	s_lshl_b64 s[38:39], s[40:41], 4
	s_add_u32 s42, s16, s38
	s_addc_u32 s43, s17, s39
	global_load_dwordx4 v[14:17], v1, s[42:43]
	s_add_u32 s42, s14, s38
	s_addc_u32 s43, s15, s39
	s_add_u32 s38, s5, s38
	s_addc_u32 s39, s6, s39
	global_load_dwordx4 v[10:13], v1, s[42:43]
	global_load_dwordx4 v[18:21], v1, s[38:39]
	s_waitcnt vmcnt(0)
	v_lshlrev_b32_e32 v50, 3, v194
	v_ashrrev_i32_e32 v51, 31, v50
	v_lshl_add_u64 v[26:27], v[50:51], 1, s[26:27]
	s_mov_b64 s[38:39], 0x26000000
	v_lshl_add_u64 v[52:53], v[26:27], 0, s[38:39]
	v_lshl_add_u64 v[28:29], s[26:27], 0, v[50:51]
	s_mov_b64 s[38:39], 0x42000000
	s_waitcnt vmcnt(14)
	v_lshl_add_u64 v[54:55], v[28:29], 0, s[38:39]
	s_mov_b64 s[38:39], 0x2a000000
	v_lshl_add_u64 v[56:57], v[26:27], 0, s[38:39]
	v_cmp_eq_u32_e64 s[38:39], 0, v194
	v_lshl_add_u64 v[58:59], v[50:51], 2, s[36:37]
	global_load_dwordx4 v[136:139], v[58:59], off offset:2048
	global_load_dwordx4 v[140:143], v[58:59], off offset:2064
	global_load_dwordx4 v[144:147], v[58:59], off
	global_load_dwordx4 v[148:151], v[58:59], off offset:16
	s_branch .LBB0_641

.LBB0_647:
	v_pk_mul_f32 v[44:45], v[82:83], v[0:1] op_sel_hi:[1,0]
	v_pk_mul_f32 v[86:87], v[38:39], v[0:1] op_sel_hi:[1,0]
	v_pk_mul_f32 v[42:43], v[42:43], v[0:1] op_sel_hi:[1,0]
	s_lshl_b64 s[40:41], s[40:41], 12
	v_pk_mul_f32 v[48:49], v[48:49], v[0:1] op_sel_hi:[1,0]
	v_pk_mul_f32 v[46:47], v[46:47], v[0:1] op_sel_hi:[1,0]
	v_pk_mul_f32 v[40:41], v[42:43], v[138:139]
	v_pk_mul_f32 v[82:83], v[44:45], v[140:141]
	v_pk_mul_f32 v[44:45], v[76:77], v[0:1] op_sel_hi:[1,0]
	v_pk_mul_f32 v[84:85], v[86:87], v[142:143]
	v_pk_mul_f32 v[38:39], v[44:45], v[136:137]
	s_load_dwordx2 s[42:43], s[0:1], 0x90
	v_pk_mul_f32 v[76:77], v[80:81], v[0:1] op_sel_hi:[1,0]
	s_waitcnt lgkmcnt(0)
	s_add_u32 s40, s42, s40
	s_addc_u32 s41, s43, s41
	v_pk_mul_f32 v[44:45], v[46:47], v[146:147]
	v_pk_mul_f32 v[88:89], v[48:49], v[150:151]
	v_pk_mul_f32 v[48:49], v[78:79], v[0:1] op_sel_hi:[1,0]
	v_lshl_add_u64 v[46:47], v[50:51], 2, s[40:41]
	v_pk_mul_f32 v[42:43], v[48:49], v[144:145]
	v_pk_mul_f32 v[86:87], v[76:77], v[148:149]
	global_store_dwordx4 v[46:47], v[42:45], off
	global_store_dwordx4 v[46:47], v[86:89], off offset:16
	global_store_dwordx4 v[46:47], v[38:41], off offset:2048
	global_store_dwordx4 v[46:47], v[82:85], off offset:2064
	s_cmpk_gt_i32 s36, 0x3fff
	s_cbranch_scc1 .LBB0_640

.LBB0_652:
	s_andn2_b64 vcc, exec, s[40:41]
	s_cbranch_vccnz .LBB0_640
	v_pk_mul_f32 v[32:33], v[44:45], v[0:1] op_sel_hi:[1,0]
	v_pk_mul_f32 v[48:49], v[22:23], v[0:1] op_sel_hi:[1,0]
	v_pk_mul_f32 v[30:31], v[30:31], v[0:1] op_sel_hi:[1,0]
	s_ashr_i32 s37, s36, 31
	s_lshl_b64 s[42:43], s[36:37], 12
	v_pk_mul_f32 v[36:37], v[36:37], v[0:1] op_sel_hi:[1,0]
	v_pk_mul_f32 v[34:35], v[34:35], v[0:1] op_sel_hi:[1,0]
	v_pk_mul_f32 v[24:25], v[30:31], v[138:139]
	v_pk_mul_f32 v[44:45], v[32:33], v[140:141]
	v_pk_mul_f32 v[32:33], v[42:43], v[0:1] op_sel_hi:[1,0]
	v_pk_mul_f32 v[46:47], v[48:49], v[142:143]
	v_pk_mul_f32 v[22:23], v[32:33], v[136:137]
	v_pk_mul_f32 v[48:49], v[40:41], v[0:1] op_sel_hi:[1,0]
	s_load_dwordx2 s[40:41], s[0:1], 0x90
	s_waitcnt lgkmcnt(0)
	s_add_u32 s40, s40, s42
	s_addc_u32 s41, s41, s43
	v_pk_mul_f32 v[32:33], v[34:35], v[146:147]
	v_pk_mul_f32 v[42:43], v[36:37], v[150:151]
	v_pk_mul_f32 v[36:37], v[38:39], v[0:1] op_sel_hi:[1,0]
	v_lshl_add_u64 v[34:35], v[50:51], 2, s[40:41]
	v_pk_mul_f32 v[30:31], v[36:37], v[144:145]
	v_pk_mul_f32 v[40:41], v[48:49], v[148:149]
	global_store_dwordx4 v[34:35], v[30:33], off
	global_store_dwordx4 v[34:35], v[40:43], off offset:16
	global_store_dwordx4 v[34:35], v[22:25], off offset:2048
	global_store_dwordx4 v[34:35], v[44:47], off offset:2064
	s_branch .LBB0_640
